# PEER U gather loop: first-half wait ladder counts the 16 loads just issued (vmcnt 31..16) so the next batch stays in flight; counted vmcnt(16) before the second half uses it
# baseline (speedup 1.0000x reference)
; #define PL_LOAD(RB, TAB, SE, BB) do { _Pragma("unroll") for (int _q = 0; _q < 16; ++_q) { \
;         const unsigned _pw = (unsigned)__builtin_amdgcn_readlane((int)(SE), (BB) * 8 + (_q >> 1)); const unsigned _idx = (_q & 1) ? (_pw >> 16) : (_pw & 0xffffu); \
;         (RB)[_q] = *(const v4u*)((TAB) + (size_t)_idx * 1024 + 16 * lane); } } while (0)
; __device__ __forceinline__ void peer_unit(Frame& F, const Args& a, int layer, int unit, bool last) {
;     ...
;             if (lt < 16) PL_LOAD(rb, U8, seL, lb);
.LBB0_1735:
	s_cmp_gt_i32 s59, 15
	s_cbranch_scc1 .Lpu_skip1
	s_lshl_b32 s46, s60, 3
	s_waitcnt lgkmcnt(0)
	v_readlane_b32 s47, v153, s46
	s_lshl_b32 s30, s47, 10
	s_and_b32 s30, s30, 0x3fffc00
	v_lshl_add_u64 v[4:5], v[140:141], 0, s[30:31]
	s_bfe_u32 s30, s47, 0x100010
	s_lshl_b32 s30, s30, 10
	v_lshl_add_u64 v[8:9], v[140:141], 0, s[30:31]
	s_or_b32 s30, s46, 1
	v_readlane_b32 s47, v153, s30
	s_lshl_b32 s30, s47, 10
	s_and_b32 s30, s30, 0x3fffc00
	v_lshl_add_u64 v[12:13], v[140:141], 0, s[30:31]
	s_bfe_u32 s30, s47, 0x100010
	s_lshl_b32 s30, s30, 10
	v_lshl_add_u64 v[16:17], v[140:141], 0, s[30:31]
	s_or_b32 s30, s46, 2
	v_readlane_b32 s47, v153, s30
	s_lshl_b32 s30, s47, 10
	s_and_b32 s30, s30, 0x3fffc00
	v_lshl_add_u64 v[20:21], v[140:141], 0, s[30:31]
	s_bfe_u32 s30, s47, 0x100010
	s_lshl_b32 s30, s30, 10
	v_lshl_add_u64 v[24:25], v[140:141], 0, s[30:31]
	s_or_b32 s30, s46, 3
	v_readlane_b32 s47, v153, s30
	s_lshl_b32 s30, s47, 10
	s_and_b32 s30, s30, 0x3fffc00
	v_lshl_add_u64 v[28:29], v[140:141], 0, s[30:31]
	s_bfe_u32 s30, s47, 0x100010
	s_lshl_b32 s30, s30, 10
	v_lshl_add_u64 v[32:33], v[140:141], 0, s[30:31]
	s_or_b32 s30, s46, 4
	v_readlane_b32 s47, v153, s30
	s_lshl_b32 s30, s47, 10
	s_and_b32 s30, s30, 0x3fffc00
	v_lshl_add_u64 v[36:37], v[140:141], 0, s[30:31]
	s_bfe_u32 s30, s47, 0x100010
	s_lshl_b32 s30, s30, 10
	v_lshl_add_u64 v[40:41], v[140:141], 0, s[30:31]
	s_or_b32 s30, s46, 5
	v_readlane_b32 s47, v153, s30
	s_lshl_b32 s30, s47, 10
	s_and_b32 s30, s30, 0x3fffc00
	v_lshl_add_u64 v[44:45], v[140:141], 0, s[30:31]
	s_bfe_u32 s30, s47, 0x100010
	s_lshl_b32 s30, s30, 10
	v_lshl_add_u64 v[48:49], v[140:141], 0, s[30:31]
	s_or_b32 s30, s46, 6
	v_readlane_b32 s47, v153, s30
	s_lshl_b32 s30, s47, 10
	s_and_b32 s30, s30, 0x3fffc00
	v_lshl_add_u64 v[52:53], v[140:141], 0, s[30:31]
	s_bfe_u32 s30, s47, 0x100010
	s_lshl_b32 s30, s30, 10
	v_lshl_add_u64 v[56:57], v[140:141], 0, s[30:31]
	s_or_b32 s30, s46, 7
	v_readlane_b32 s46, v153, s30
	s_lshl_b32 s30, s46, 10
	s_and_b32 s30, s30, 0x3fffc00
	v_lshl_add_u64 v[60:61], v[140:141], 0, s[30:31]
	s_bfe_u32 s30, s46, 0x100010
	s_lshl_b32 s30, s30, 10
	v_lshl_add_u64 v[64:65], v[140:141], 0, s[30:31]
	global_load_dwordx4 v[4:7], v[4:5], off
	s_nop 0
	global_load_dwordx4 v[8:11], v[8:9], off
	s_nop 0
	global_load_dwordx4 v[12:15], v[12:13], off
	s_nop 0
	global_load_dwordx4 v[16:19], v[16:17], off
	s_nop 0
	global_load_dwordx4 v[20:23], v[20:21], off
	s_nop 0
	global_load_dwordx4 v[24:27], v[24:25], off
	s_nop 0
	global_load_dwordx4 v[28:31], v[28:29], off
	s_nop 0
	global_load_dwordx4 v[32:35], v[32:33], off
	s_nop 0
	global_load_dwordx4 v[36:39], v[36:37], off
	s_nop 0
	global_load_dwordx4 v[40:43], v[40:41], off
	s_nop 0
	global_load_dwordx4 v[44:47], v[44:45], off
	s_nop 0
	global_load_dwordx4 v[48:51], v[48:49], off
	s_nop 0
	global_load_dwordx4 v[52:55], v[52:53], off
	s_nop 0
	global_load_dwordx4 v[56:59], v[56:57], off
	s_nop 0
	global_load_dwordx4 v[60:63], v[60:61], off
	s_nop 0
	global_load_dwordx4 v[64:67], v[64:65], off
	s_branch .Lpu_go1

; #define PL_LOAD(RB, TAB, SE, BB) do { _Pragma("unroll") for (int _q = 0; _q < 16; ++_q) { \
;         const unsigned _pw = (unsigned)__builtin_amdgcn_readlane((int)(SE), (BB) * 8 + (_q >> 1)); const unsigned _idx = (_q & 1) ? (_pw >> 16) : (_pw & 0xffffu); \
;         (RB)[_q] = *(const v4u*)((TAB) + (size_t)_idx * 1024 + 16 * lane); } } while (0)
; __device__ __forceinline__ void peer_unit(Frame& F, const Args& a, int layer, int unit, bool last) {
;     ...
;             if (lt < 16) PL_LOAD(rb, U8, seL, lb);
;             U_COMPUTE(ra);
.Lpu_go1:
.LBB0_1737:
	s_cmp_lg_u32 s48, s56
	s_cbranch_scc1 .LBB0_1741
	s_waitcnt vmcnt(16)
	v_mov_b64_e32 v[138:139], v[70:71]
	s_cmp_eq_u32 s58, 15
	v_mov_b64_e32 v[136:137], v[68:69]
	s_cbranch_scc1 .LBB0_1740
	s_ashr_i32 s30, s58, 31
	s_add_u32 s46, s0, s58
	s_addc_u32 s47, s1, s30
	s_lshl_b64 s[46:47], s[46:47], 10
	v_lshl_add_u64 v[136:137], v[144:145], 0, s[46:47]
	global_load_dwordx4 v[136:139], v[136:137], off offset:1024

.LBB0_1741:
	s_waitcnt vmcnt(31)
	v_mfma_f32_16x16x32_fp8_fp8 v[154:157], v[72:73], v[148:149], 0
	s_lshl_b32 s30, s58, 9
	v_lshl_add_u32 v136, s48, 4, v152
	s_add_i32 s30, s15, s30
	v_mfma_f32_16x16x32_fp8_fp8 v[154:157], v[74:75], v[146:147], v[154:157]
	s_nop 7
	v_cndmask_b32_e64 v137, v157, v156, s[42:43]
	v_cndmask_b32_e64 v138, v155, v154, s[42:43]
	s_waitcnt vmcnt(30)
	v_mfma_f32_16x16x32_fp8_fp8 v[154:157], v[76:77], v[148:149], 0
	v_cndmask_b32_e64 v137, v137, v138, s[40:41]
	v_cndmask_b32_e64 v137, 0, v137, s[38:39]
	v_mfma_f32_16x16x32_fp8_fp8 v[154:157], v[78:79], v[146:147], v[154:157]
	s_nop 7
	v_cndmask_b32_e64 v138, v157, v156, s[42:43]
	v_cndmask_b32_e64 v139, v155, v154, s[42:43]
	s_waitcnt vmcnt(29)
	v_mfma_f32_16x16x32_fp8_fp8 v[154:157], v[80:81], v[148:149], 0
	v_cndmask_b32_e64 v138, v138, v139, s[40:41]
	v_cndmask_b32_e64 v138, 0, v138, s[38:39]
	v_mfma_f32_16x16x32_fp8_fp8 v[154:157], v[82:83], v[146:147], v[154:157]
	s_nop 7
	v_cndmask_b32_e64 v139, v157, v156, s[42:43]
	v_cndmask_b32_e64 v154, v155, v154, s[42:43]
	v_cndmask_b32_e64 v139, v139, v154, s[40:41]
	s_waitcnt vmcnt(28)
	v_mfma_f32_16x16x32_fp8_fp8 v[154:157], v[84:85], v[148:149], 0
	v_cndmask_b32_e64 v139, 0, v139, s[38:39]
	v_mfma_f32_16x16x32_fp8_fp8 v[154:157], v[86:87], v[146:147], v[154:157]
	s_nop 7
	v_cndmask_b32_e64 v156, v157, v156, s[42:43]
	v_cndmask_b32_e64 v154, v155, v154, s[42:43]
	v_cndmask_b32_e64 v158, v156, v154, s[40:41]
	s_waitcnt vmcnt(27)
	v_mfma_f32_16x16x32_fp8_fp8 v[154:157], v[88:89], v[148:149], 0
	v_mfma_f32_16x16x32_fp8_fp8 v[154:157], v[90:91], v[146:147], v[154:157]
	s_nop 7
	v_cndmask_b32_e64 v156, v157, v156, s[42:43]
	v_cndmask_b32_e64 v154, v155, v154, s[42:43]
	v_cndmask_b32_e64 v159, v156, v154, s[40:41]
	s_waitcnt vmcnt(26)
	v_mfma_f32_16x16x32_fp8_fp8 v[154:157], v[92:93], v[148:149], 0
	v_mfma_f32_16x16x32_fp8_fp8 v[154:157], v[94:95], v[146:147], v[154:157]
	s_nop 7
	v_cndmask_b32_e64 v156, v157, v156, s[42:43]
	v_cndmask_b32_e64 v154, v155, v154, s[42:43]
	v_cndmask_b32_e64 v160, v156, v154, s[40:41]
	s_waitcnt vmcnt(25)
	v_mfma_f32_16x16x32_fp8_fp8 v[154:157], v[96:97], v[148:149], 0
	v_mfma_f32_16x16x32_fp8_fp8 v[154:157], v[98:99], v[146:147], v[154:157]
	s_nop 7
	v_cndmask_b32_e64 v156, v157, v156, s[42:43]
	v_cndmask_b32_e64 v154, v155, v154, s[42:43]
	v_cndmask_b32_e64 v161, v156, v154, s[40:41]
	s_waitcnt vmcnt(24)
	v_mfma_f32_16x16x32_fp8_fp8 v[154:157], v[100:101], v[148:149], 0
	v_mfma_f32_16x16x32_fp8_fp8 v[154:157], v[102:103], v[146:147], v[154:157]
	s_nop 7
	v_cndmask_b32_e64 v154, v155, v154, s[42:43]
	v_cndmask_b32_e64 v155, 0, v159, s[38:39]
	s_nop 1
	v_permlane32_swap_b32_e32 v137, v155
	v_add_f32_e32 v137, v137, v155
	v_cndmask_b32_e64 v155, 0, v160, s[38:39]
	s_nop 1
	v_permlane32_swap_b32_e32 v138, v155
	v_add_f32_e32 v138, v138, v155
	v_cndmask_b32_e64 v155, 0, v161, s[38:39]
	v_cndmask_b32_e64 v156, v157, v156, s[42:43]
	s_nop 0
	v_permlane32_swap_b32_e32 v139, v155
	v_cndmask_b32_e64 v154, v156, v154, s[40:41]
	v_add_f32_e32 v139, v139, v155
	v_cndmask_b32_e64 v155, 0, v158, s[38:39]
	v_cndmask_b32_e64 v154, 0, v154, s[38:39]
	v_permlane16_swap_b32_e32 v137, v139
	s_nop 0
	v_permlane32_swap_b32_e32 v155, v154
	v_add_f32_e32 v137, v137, v139
	v_add_f32_e32 v156, v155, v154
	s_nop 1
	v_permlane16_swap_b32_e32 v138, v156
	v_add_f32_dpp v137, v137, v137 row_ror:8 row_mask:0xf bank_mask:0xf bound_ctrl:1
	v_mov_b32_e32 v155, 0
	v_mov_b32_e32 v139, 0
	v_add_f32_dpp v137, v137, v137 row_ror:4 row_mask:0xf bank_mask:0xf bound_ctrl:1
	s_nop 1
	v_add_f32_dpp v154, v137, v137 row_ror:2 row_mask:0xf bank_mask:0xf bound_ctrl:1
	v_add_f32_e32 v137, v138, v156
	s_nop 0
	v_mov_b32_dpp v155, v154 row_ror:1 row_mask:0xf bank_mask:0xf
	v_add_f32_dpp v137, v137, v137 row_ror:8 row_mask:0xf bank_mask:0xf bound_ctrl:1
	s_nop 1
	v_add_f32_dpp v137, v137, v137 row_ror:4 row_mask:0xf bank_mask:0xf bound_ctrl:1
	s_nop 1
	v_add_f32_dpp v138, v137, v137 row_ror:2 row_mask:0xf bank_mask:0xf bound_ctrl:1
	v_lshl_add_u32 v137, v136, 2, s30
	s_nop 0
	v_mov_b32_dpp v139, v138 row_ror:1 row_mask:0xf bank_mask:0xf
	s_and_saveexec_b64 s[56:57], s[44:45]
	s_cbranch_execz .LBB0_1746
	v_cmp_le_i32_e32 vcc, s70, v136
	v_cmp_gt_i32_e64 s[46:47], s61, v136
	s_and_b64 s[72:73], vcc, s[46:47]
	s_and_saveexec_b64 s[46:47], s[72:73]
	s_cbranch_execz .LBB0_1744
	v_add_f32_e32 v154, v154, v155
	v_mul_f32_e32 v154, 0x39800000, v154
	v_mul_f32_e32 v155, 0x3d372713, v154
	v_mul_f32_e32 v155, v154, v155
	v_fma_f32 v155, v154, v155, v154
	v_mul_f32_e32 v155, 0x3fcc422a, v155
	v_mul_f32_e32 v155, 0xbfb8aa3b, v155
	v_exp_f32_e32 v155, v155
	s_nop 0
	v_add_f32_e32 v155, 1.0, v155
	v_rcp_f32_e32 v155, v155
	s_nop 0
	v_mul_f32_e32 v154, v154, v155
	ds_read_b32 v155, v137
	v_mul_f32_e32 v154, 0x3c800000, v154
	s_waitcnt lgkmcnt(0)
	v_mul_f32_e32 v154, v154, v155
	ds_write_b32 v137, v154

.LBB0_1746:
	s_or_b64 exec, exec, s[56:57]
	s_waitcnt vmcnt(23)
	v_mfma_f32_16x16x32_fp8_fp8 v[154:157], v[104:105], v[148:149], 0
	v_mfma_f32_16x16x32_fp8_fp8 v[154:157], v[106:107], v[146:147], v[154:157]
	s_nop 7
	v_cndmask_b32_e64 v138, v157, v156, s[42:43]
	v_cndmask_b32_e64 v139, v155, v154, s[42:43]
	s_waitcnt vmcnt(22)
	v_mfma_f32_16x16x32_fp8_fp8 v[154:157], v[108:109], v[148:149], 0
	v_cndmask_b32_e64 v138, v138, v139, s[40:41]
	v_cndmask_b32_e64 v138, 0, v138, s[38:39]
	v_mfma_f32_16x16x32_fp8_fp8 v[154:157], v[110:111], v[146:147], v[154:157]
	s_nop 7
	v_cndmask_b32_e64 v139, v157, v156, s[42:43]
	v_cndmask_b32_e64 v154, v155, v154, s[42:43]
	v_cndmask_b32_e64 v139, v139, v154, s[40:41]
	s_waitcnt vmcnt(21)
	v_mfma_f32_16x16x32_fp8_fp8 v[154:157], v[112:113], v[148:149], 0
	v_cndmask_b32_e64 v139, 0, v139, s[38:39]
	v_mfma_f32_16x16x32_fp8_fp8 v[154:157], v[114:115], v[146:147], v[154:157]
	s_nop 7
	v_cndmask_b32_e64 v156, v157, v156, s[42:43]
	v_cndmask_b32_e64 v154, v155, v154, s[42:43]
	v_cndmask_b32_e64 v158, v156, v154, s[40:41]
	s_waitcnt vmcnt(20)
	v_mfma_f32_16x16x32_fp8_fp8 v[154:157], v[116:117], v[148:149], 0
	v_mfma_f32_16x16x32_fp8_fp8 v[154:157], v[118:119], v[146:147], v[154:157]
	s_nop 7
	v_cndmask_b32_e64 v156, v157, v156, s[42:43]
	v_cndmask_b32_e64 v154, v155, v154, s[42:43]
	v_cndmask_b32_e64 v159, v156, v154, s[40:41]
	s_waitcnt vmcnt(19)
	v_mfma_f32_16x16x32_fp8_fp8 v[154:157], v[120:121], v[148:149], 0
	v_mfma_f32_16x16x32_fp8_fp8 v[154:157], v[122:123], v[146:147], v[154:157]
	s_nop 7
	v_cndmask_b32_e64 v156, v157, v156, s[42:43]
	v_cndmask_b32_e64 v154, v155, v154, s[42:43]
	v_cndmask_b32_e64 v160, v156, v154, s[40:41]
	s_waitcnt vmcnt(18)
	v_mfma_f32_16x16x32_fp8_fp8 v[154:157], v[124:125], v[148:149], 0
	v_mfma_f32_16x16x32_fp8_fp8 v[154:157], v[126:127], v[146:147], v[154:157]
	s_nop 7
	v_cndmask_b32_e64 v156, v157, v156, s[42:43]
	v_cndmask_b32_e64 v154, v155, v154, s[42:43]
	v_cndmask_b32_e64 v161, v156, v154, s[40:41]
	s_waitcnt vmcnt(17)
	v_mfma_f32_16x16x32_fp8_fp8 v[154:157], v[128:129], v[148:149], 0
	v_mfma_f32_16x16x32_fp8_fp8 v[154:157], v[130:131], v[146:147], v[154:157]
	s_nop 7
	v_cndmask_b32_e64 v156, v157, v156, s[42:43]
	v_cndmask_b32_e64 v154, v155, v154, s[42:43]
	v_cndmask_b32_e64 v162, v156, v154, s[40:41]
	s_waitcnt vmcnt(16)
	v_mfma_f32_16x16x32_fp8_fp8 v[154:157], v[132:133], v[148:149], 0
	v_mfma_f32_16x16x32_fp8_fp8 v[154:157], v[134:135], v[146:147], v[154:157]
	s_nop 7
	v_cndmask_b32_e64 v154, v155, v154, s[42:43]
	v_cndmask_b32_e64 v155, 0, v160, s[38:39]
	s_nop 1
	v_permlane32_swap_b32_e32 v138, v155
	v_add_f32_e32 v138, v138, v155
	v_cndmask_b32_e64 v155, 0, v161, s[38:39]
	v_cndmask_b32_e64 v156, v157, v156, s[42:43]
	s_nop 0
	v_permlane32_swap_b32_e32 v139, v155
	v_cndmask_b32_e64 v154, v156, v154, s[40:41]
	v_add_f32_e32 v139, v139, v155
	v_cndmask_b32_e64 v155, 0, v158, s[38:39]
	v_cndmask_b32_e64 v156, 0, v162, s[38:39]
	s_nop 1
	v_permlane32_swap_b32_e32 v155, v156
	v_add_f32_e32 v155, v155, v156
	v_cndmask_b32_e64 v156, 0, v159, s[38:39]
	v_cndmask_b32_e64 v154, 0, v154, s[38:39]
	v_permlane16_swap_b32_e32 v138, v155
	s_nop 0
	v_permlane32_swap_b32_e32 v156, v154
	v_add_f32_e32 v138, v138, v155
	v_add_f32_e32 v156, v156, v154
	s_nop 1
	v_permlane16_swap_b32_e32 v139, v156
	v_add_f32_dpp v138, v138, v138 row_ror:8 row_mask:0xf bank_mask:0xf bound_ctrl:1
	v_mov_b32_e32 v155, 0
	s_nop 0
	v_add_f32_dpp v138, v138, v138 row_ror:4 row_mask:0xf bank_mask:0xf bound_ctrl:1
	s_nop 1
	v_add_f32_dpp v154, v138, v138 row_ror:2 row_mask:0xf bank_mask:0xf bound_ctrl:1
	v_add_f32_e32 v138, v139, v156
	v_mov_b32_e32 v139, 0
	v_mov_b32_dpp v155, v154 row_ror:1 row_mask:0xf bank_mask:0xf
	v_add_f32_dpp v138, v138, v138 row_ror:8 row_mask:0xf bank_mask:0xf bound_ctrl:1
	s_nop 1
	v_add_f32_dpp v138, v138, v138 row_ror:4 row_mask:0xf bank_mask:0xf bound_ctrl:1
	s_nop 1
	v_add_f32_dpp v138, v138, v138 row_ror:2 row_mask:0xf bank_mask:0xf bound_ctrl:1
	s_nop 1
	v_mov_b32_dpp v139, v138 row_ror:1 row_mask:0xf bank_mask:0xf
	s_and_saveexec_b64 s[56:57], s[44:45]
	s_cbranch_execz .LBB0_1751
	v_add_u32_e32 v136, 8, v136
	v_cmp_le_i32_e32 vcc, s70, v136
	v_cmp_gt_i32_e64 s[46:47], s61, v136
	s_and_b64 s[72:73], vcc, s[46:47]
	s_and_saveexec_b64 s[46:47], s[72:73]
	s_cbranch_execz .LBB0_1749
	v_add_f32_e32 v154, v154, v155
	v_mul_f32_e32 v154, 0x39800000, v154
	v_mul_f32_e32 v155, 0x3d372713, v154
	v_mul_f32_e32 v155, v154, v155
	v_fma_f32 v155, v154, v155, v154
	v_mul_f32_e32 v155, 0x3fcc422a, v155
	v_mul_f32_e32 v155, 0xbfb8aa3b, v155
	v_exp_f32_e32 v155, v155
	s_nop 0
	v_add_f32_e32 v155, 1.0, v155
	v_rcp_f32_e32 v155, v155
	s_nop 0
	v_mul_f32_e32 v154, v154, v155
	ds_read_b32 v155, v137 offset:32
	v_mul_f32_e32 v154, 0x3c800000, v154
	s_waitcnt lgkmcnt(0)
	v_mul_f32_e32 v154, v154, v155
	ds_write_b32 v137, v154 offset:32

; #define PL_LOAD(RB, TAB, SE, BB) do { _Pragma("unroll") for (int _q = 0; _q < 16; ++_q) { \
;         const unsigned _pw = (unsigned)__builtin_amdgcn_readlane((int)(SE), (BB) * 8 + (_q >> 1)); const unsigned _idx = (_q & 1) ? (_pw >> 16) : (_pw & 0xffffu); \
;         (RB)[_q] = *(const v4u*)((TAB) + (size_t)_idx * 1024 + 16 * lane); } } while (0)
; __device__ __forceinline__ void peer_unit(Frame& F, const Args& a, int layer, int unit, bool last) {
;     ...
;             if (lt < 16) PL_LOAD(ra, U8, seL, lb);
.LBB0_1756:
	s_cmp_gt_i32 s58, 15
	s_cbranch_scc1 .LBB0_1758
	s_lshl_b32 s47, s48, 3
	s_waitcnt lgkmcnt(0)
	v_readlane_b32 s56, v153, s47
	s_lshl_b32 s30, s56, 10
	s_and_b32 s30, s30, 0x3fffc00
	v_lshl_add_u64 v[72:73], v[140:141], 0, s[30:31]
	s_bfe_u32 s30, s56, 0x100010
	s_lshl_b32 s30, s30, 10
	v_lshl_add_u64 v[76:77], v[140:141], 0, s[30:31]
	s_or_b32 s30, s47, 1
	v_readlane_b32 s56, v153, s30
	s_lshl_b32 s30, s56, 10
	s_and_b32 s30, s30, 0x3fffc00
	v_lshl_add_u64 v[80:81], v[140:141], 0, s[30:31]
	s_bfe_u32 s30, s56, 0x100010
	s_lshl_b32 s30, s30, 10
	v_lshl_add_u64 v[84:85], v[140:141], 0, s[30:31]
	s_or_b32 s30, s47, 2
	v_readlane_b32 s56, v153, s30
	s_lshl_b32 s30, s56, 10
	s_and_b32 s30, s30, 0x3fffc00
	v_lshl_add_u64 v[88:89], v[140:141], 0, s[30:31]
	s_bfe_u32 s30, s56, 0x100010
	s_lshl_b32 s30, s30, 10
	v_lshl_add_u64 v[92:93], v[140:141], 0, s[30:31]
	s_or_b32 s30, s47, 3
	v_readlane_b32 s56, v153, s30
	s_lshl_b32 s30, s56, 10
	s_and_b32 s30, s30, 0x3fffc00
	v_lshl_add_u64 v[96:97], v[140:141], 0, s[30:31]
	s_bfe_u32 s30, s56, 0x100010
	s_lshl_b32 s30, s30, 10
	v_lshl_add_u64 v[100:101], v[140:141], 0, s[30:31]
	s_or_b32 s30, s47, 4
	v_readlane_b32 s56, v153, s30
	s_lshl_b32 s30, s56, 10
	s_and_b32 s30, s30, 0x3fffc00
	v_lshl_add_u64 v[104:105], v[140:141], 0, s[30:31]
	s_bfe_u32 s30, s56, 0x100010
	s_lshl_b32 s30, s30, 10
	v_lshl_add_u64 v[108:109], v[140:141], 0, s[30:31]
	s_or_b32 s30, s47, 5
	v_readlane_b32 s56, v153, s30
	s_lshl_b32 s30, s56, 10
	s_and_b32 s30, s30, 0x3fffc00
	v_lshl_add_u64 v[112:113], v[140:141], 0, s[30:31]
	s_bfe_u32 s30, s56, 0x100010
	s_lshl_b32 s30, s30, 10
	v_lshl_add_u64 v[116:117], v[140:141], 0, s[30:31]
	s_or_b32 s30, s47, 6
	v_readlane_b32 s56, v153, s30
	s_lshl_b32 s30, s56, 10
	s_and_b32 s30, s30, 0x3fffc00
	v_lshl_add_u64 v[120:121], v[140:141], 0, s[30:31]
	s_bfe_u32 s30, s56, 0x100010
	s_lshl_b32 s30, s30, 10
	v_lshl_add_u64 v[124:125], v[140:141], 0, s[30:31]
	s_or_b32 s30, s47, 7
	v_readlane_b32 s47, v153, s30
	s_lshl_b32 s30, s47, 10
	s_and_b32 s30, s30, 0x3fffc00
	v_lshl_add_u64 v[128:129], v[140:141], 0, s[30:31]
	s_bfe_u32 s30, s47, 0x100010
	s_lshl_b32 s30, s30, 10
	v_lshl_add_u64 v[132:133], v[140:141], 0, s[30:31]
	global_load_dwordx4 v[72:75], v[72:73], off
	s_nop 0
	global_load_dwordx4 v[76:79], v[76:77], off
	s_nop 0
	global_load_dwordx4 v[80:83], v[80:81], off
	s_nop 0
	global_load_dwordx4 v[84:87], v[84:85], off
	s_nop 0
	global_load_dwordx4 v[88:91], v[88:89], off
	s_nop 0
	global_load_dwordx4 v[92:95], v[92:93], off
	s_nop 0
	global_load_dwordx4 v[96:99], v[96:97], off
	s_nop 0
	global_load_dwordx4 v[100:103], v[100:101], off
	s_nop 0
	global_load_dwordx4 v[104:107], v[104:105], off
	s_nop 0
	global_load_dwordx4 v[108:111], v[108:109], off
	s_nop 0
	global_load_dwordx4 v[112:115], v[112:113], off
	s_nop 0
	global_load_dwordx4 v[116:119], v[116:117], off
	s_nop 0
	global_load_dwordx4 v[120:123], v[120:121], off
	s_nop 0
	global_load_dwordx4 v[124:127], v[124:125], off
	s_nop 0
	global_load_dwordx4 v[128:131], v[128:129], off
	s_nop 0
	global_load_dwordx4 v[132:135], v[132:133], off
	s_waitcnt vmcnt(16)
	s_branch .Lpu_go2
.LBB0_1758:
	s_waitcnt vmcnt(0)
.Lpu_go2:
	s_and_b32 s30, s46, 0xff
	s_add_i32 s30, s30, 15
	s_and_b32 s30, s30, 0x1f0
	s_min_u32 s47, s30, 0x80
	s_bfe_u32 s30, s46, 0x80008
	s_add_i32 s30, s30, 15
	s_and_b32 s30, s30, 0x1f0
	s_min_u32 s56, s30, 0x80
	s_bfe_u32 s30, s46, 0x80010
	s_add_i32 s30, s30, 15
	s_and_b32 s30, s30, 0x1f0
	s_min_u32 s46, s30, 0x80
	s_and_b64 s[70:71], s[6:7], exec
	s_cselect_b32 s30, s56, s46
	s_and_b64 s[70:71], s[52:53], exec
	s_cselect_b32 s30, s47, s30
	s_and_b64 s[70:71], s[54:55], exec
	s_cselect_b32 s30, 0, s30
	s_lshr_b32 s57, s30, 4
	s_min_u32 s57, s57, 7
	s_cmp_lg_u32 s60, s57
	s_cbranch_scc1 .LBB0_1762
	v_mov_b64_e32 v[138:139], v[70:71]
	s_cmp_eq_u32 s59, 15
	v_mov_b64_e32 v[136:137], v[68:69]
	s_cbranch_scc1 .LBB0_1761
	s_ashr_i32 s57, s59, 31
	s_add_u32 s70, s0, s59
	s_addc_u32 s71, s1, s57
	s_lshl_b64 s[70:71], s[70:71], 10
	v_lshl_add_u64 v[136:137], v[144:145], 0, s[70:71]
	global_load_dwordx4 v[136:139], v[136:137], off offset:1024
